# top-k prefix scans via DPP row_shr/row_bcast instead of ds_bpermute butterflies (on top of v8)
# speedup vs baseline: 1.0112x; 1.0112x over previous
; #define LAS __attribute__((address_space(3)))
; __device__ __forceinline__ unsigned block_excl_scan(unsigned cnt, LAS unsigned* wsum, int tid) {
;     const int lane = tid & 63, wv = tid >> 6;
;     unsigned inc = cnt;
; #pragma unroll
;     for (int o = 1; o < 64; o <<= 1) { const unsigned t = __shfl_up(inc, o); if (lane >= o) inc += t; }
;     if (lane == 63) wsum[wv] = inc;
;     __syncthreads();
;     unsigned base = 0;
; #pragma unroll
;     for (int w = 0; w < 8; ++w) base += (w < wv) ? wsum[w] : 0u;
;     __syncthreads();
; __device__ __forceinline__ void ph_topk(const Params& p, LAS unsigned char* lds, const unsigned* done = nullptr) {
;     ...
; #pragma unroll 1
;         for (int pass = 0; pass < 4; ++pass) {
;             const int shift = 24 - 8 * pass;
;             if (tid < 256) hist[tid] = 0;
;             __syncthreads();
; #pragma unroll
;             for (int i = 0; i < 4; ++i) if (pass == 0 || (k[i] >> (shift + 8)) == prefix) __hip_atomic_fetch_add(&hist[(k[i] >> shift) & 255u], 1u, __ATOMIC_RELAXED, __HIP_MEMORY_SCOPE_WORKGROUP);
;             __syncthreads();
;             { const unsigned cnt = (tid < 256) ? hist[255 - tid] : 0u;
;               const unsigned Sn = block_excl_scan(cnt, wsum, tid), S = Sn + cnt;
;               if (tid < 256 && S >= krem && Sn < krem) { misc[0] = (prefix << 8) | (unsigned)(255 - tid); misc[1] = krem - Sn; } }
;             __syncthreads();
;             prefix = misc[0]; krem = misc[1];
.LBB0_1519:
	s_and_saveexec_b64 s[40:41], s[68:69]
	ds_write_b32 v3, v195
	s_or_b64 exec, exec, s[40:41]
	s_add_i32 s8, s9, -8
	s_cmp_eq_u32 s9, 32
	s_waitcnt vmcnt(3)
	v_lshrrev_b32_e32 v21, s9, v14
	s_cselect_b64 s[40:41], -1, 0
	v_cmp_eq_u32_e32 vcc, v21, v6
	s_or_b64 s[10:11], s[40:41], vcc
	s_waitcnt lgkmcnt(0)
	s_barrier
	s_and_saveexec_b64 s[42:43], s[10:11]
	v_bfe_u32 v21, v14, s8, 8
	v_lshl_add_u32 v21, v21, 2, 0
	ds_add_u32 v21, v221
	s_or_b64 exec, exec, s[42:43]
	s_waitcnt vmcnt(2)
	v_lshrrev_b32_e32 v21, s9, v9
	v_cmp_eq_u32_e32 vcc, v21, v6
	s_or_b64 s[10:11], s[40:41], vcc
	s_and_saveexec_b64 s[42:43], s[10:11]
	v_bfe_u32 v21, v9, s8, 8
	v_lshl_add_u32 v21, v21, 2, 0
	ds_add_u32 v21, v221
	s_or_b64 exec, exec, s[42:43]
	s_waitcnt vmcnt(1)
	v_lshrrev_b32_e32 v21, s9, v8
	v_cmp_eq_u32_e32 vcc, v21, v6
	s_or_b64 s[10:11], s[40:41], vcc
	s_and_saveexec_b64 s[42:43], s[10:11]
	v_bfe_u32 v21, v8, s8, 8
	v_lshl_add_u32 v21, v21, 2, 0
	ds_add_u32 v21, v221
	s_or_b64 exec, exec, s[42:43]
	s_waitcnt vmcnt(0)
	v_lshrrev_b32_e32 v21, s9, v13
	v_cmp_eq_u32_e32 vcc, v21, v6
	s_or_b64 s[10:11], s[40:41], vcc
	s_and_saveexec_b64 s[40:41], s[10:11]
	v_bfe_u32 v21, v13, s8, 8
	v_lshl_add_u32 v21, v21, 2, 0
	ds_add_u32 v21, v221
	s_or_b64 exec, exec, s[40:41]
	v_mov_b32_e32 v21, 0
	s_waitcnt lgkmcnt(0)
	s_barrier
	s_and_saveexec_b64 s[40:41], s[68:69]
	ds_read_b32 v21, v11 offset:1020
	s_or_b64 exec, exec, s[40:41]
	s_waitcnt lgkmcnt(0)
	v_mov_b32_e32 v22, v21
	s_nop 1
	v_add_u32_dpp v22, v22, v22 row_shr:1 row_mask:0xf bank_mask:0xf bound_ctrl:0
	s_nop 1
	v_add_u32_dpp v22, v22, v22 row_shr:2 row_mask:0xf bank_mask:0xf bound_ctrl:0
	s_nop 1
	v_add_u32_dpp v22, v22, v22 row_shr:4 row_mask:0xf bank_mask:0xf bound_ctrl:0
	s_nop 1
	v_add_u32_dpp v22, v22, v22 row_shr:8 row_mask:0xf bank_mask:0xf bound_ctrl:0
	s_nop 1
	v_add_u32_dpp v22, v22, v22 row_bcast:15 row_mask:0xa bank_mask:0xf
	s_nop 1
	v_add_u32_dpp v22, v22, v22 row_bcast:31 row_mask:0xc bank_mask:0xf
	s_and_saveexec_b64 s[40:41], s[82:83]
	ds_write_b32 v12, v22 offset:1280
	s_or_b64 exec, exec, s[40:41]
	v_mov_b32_e32 v23, 0
	v_mov_b32_e32 v24, 0
	s_waitcnt lgkmcnt(0)
	s_barrier
	s_and_saveexec_b64 s[40:41], s[84:85]
	ds_read_b32 v24, v195 offset:1280
	s_or_b64 exec, exec, s[40:41]
	s_and_saveexec_b64 s[40:41], s[86:87]
	ds_read_b32 v23, v195 offset:1284
	s_or_b64 exec, exec, s[40:41]
	v_mov_b32_e32 v25, 0
	v_mov_b32_e32 v26, 0
	s_and_saveexec_b64 s[40:41], s[88:89]
	ds_read_b32 v26, v195 offset:1288
	s_or_b64 exec, exec, s[40:41]
	s_and_saveexec_b64 s[40:41], s[90:91]
	ds_read_b32 v25, v195 offset:1292
	s_or_b64 exec, exec, s[40:41]
	v_mov_b32_e32 v27, 0
	v_mov_b32_e32 v28, 0
	s_and_saveexec_b64 s[40:41], s[92:93]
	ds_read_b32 v28, v195 offset:1296
	s_or_b64 exec, exec, s[40:41]
	s_and_saveexec_b64 s[40:41], s[94:95]
	ds_read_b32 v27, v195 offset:1300
	s_or_b64 exec, exec, s[40:41]
	v_mov_b32_e32 v29, 0
	v_mov_b32_e32 v30, 0
	s_and_saveexec_b64 s[40:41], s[96:97]
	ds_read_b32 v30, v195 offset:1304
	s_or_b64 exec, exec, s[40:41]
	s_and_saveexec_b64 s[40:41], s[38:39]
	ds_read_b32 v29, v195 offset:1308
	s_or_b64 exec, exec, s[40:41]
	s_waitcnt lgkmcnt(0)
	v_add_u32_e32 v23, v23, v24
	v_add3_u32 v23, v23, v26, v25
	v_add3_u32 v23, v23, v28, v27
	v_add3_u32 v23, v23, v30, v29
	v_sub_u32_e32 v21, v22, v21
	v_add_u32_e32 v22, v23, v22
	v_add_u32_e32 v21, v23, v21
	v_cmp_ge_u32_e32 vcc, v22, v7
	s_and_b64 s[10:11], s[68:69], vcc
	v_cmp_gt_u32_e32 vcc, v7, v21
	s_and_b64 s[10:11], s[10:11], vcc
	s_barrier
	s_and_saveexec_b64 s[40:41], s[10:11]
	s_cbranch_execz .LBB0_1518
	v_lshl_or_b32 v6, v6, 8, v10
	v_sub_u32_e32 v7, v7, v21
	ds_write_b64 v195, v[6:7] offset:1024
	s_branch .LBB0_1518
; #define LAS __attribute__((address_space(3)))
; __device__ __forceinline__ unsigned block_excl_scan(unsigned cnt, LAS unsigned* wsum, int tid) {
;     const int lane = tid & 63, wv = tid >> 6;
;     unsigned inc = cnt;
; #pragma unroll
;     for (int o = 1; o < 64; o <<= 1) { const unsigned t = __shfl_up(inc, o); if (lane >= o) inc += t; }
;     if (lane == 63) wsum[wv] = inc;
;     __syncthreads();
;     unsigned base = 0;
; #pragma unroll
;     for (int w = 0; w < 8; ++w) base += (w < wv) ? wsum[w] : 0u;
;     __syncthreads();
;     return base + inc - cnt;
; __device__ __forceinline__ void ph_topk(const Params& p, LAS unsigned char* lds, const unsigned* done = nullptr) {
;     ...
;         unsigned neq = 0;
; #pragma unroll
;         for (int i = 0; i < 4; ++i) neq += (k[i] == prefix) ? 1u : 0u;
;         unsigned eqbase = block_excl_scan(neq, wsum, tid);
;         unsigned sel[4]; unsigned nsel = 0;
; #pragma unroll
;         for (int i = 0; i < 4; ++i) { const bool eq = k[i] == prefix; sel[i] = (k[i] > prefix || (eq && eqbase < krem)) ? 1u : 0u; eqbase += eq ? 1u : 0u; nsel += sel[i]; }
;         unsigned sb = block_excl_scan(nsel, wsum, tid);
; #pragma unroll
;         for (int i = 0; i < 4; ++i) {
;             const int s = 4 * tid + i, t = b * 2048 + s;
;             if (sel[i]) { const int row = e * 1024 + b * 256 + (int)sb; idx[row] = t; gate[row] = a[i]; slot_of[(size_t)e * NT + t] = row; ++sb; }
;             else slot_of[(size_t)e * NT + t] = -1;
.LBB0_1551:
	v_cmp_eq_u32_e64 s[44:45], v9, v6
	v_cmp_eq_u32_e64 s[48:49], v14, v6
	v_cmp_eq_u32_e64 s[42:43], v8, v6
	v_cndmask_b32_e64 v22, 0, 1, s[44:45]
	v_addc_co_u32_e64 v23, s[40:41], 0, v22, s[48:49]
	v_cndmask_b32_e64 v21, 0, 1, s[42:43]
	v_cmp_eq_u32_e64 s[40:41], v13, v6
	s_nop 1
	v_addc_co_u32_e64 v23, vcc, v23, v21, s[40:41]
	v_mov_b32_e32 v24, v23
	s_nop 1
	v_add_u32_dpp v24, v24, v24 row_shr:1 row_mask:0xf bank_mask:0xf bound_ctrl:0
	s_nop 1
	v_add_u32_dpp v24, v24, v24 row_shr:2 row_mask:0xf bank_mask:0xf bound_ctrl:0
	s_nop 1
	v_add_u32_dpp v24, v24, v24 row_shr:4 row_mask:0xf bank_mask:0xf bound_ctrl:0
	s_nop 1
	v_add_u32_dpp v24, v24, v24 row_shr:8 row_mask:0xf bank_mask:0xf bound_ctrl:0
	s_nop 1
	v_add_u32_dpp v24, v24, v24 row_bcast:15 row_mask:0xa bank_mask:0xf
	s_nop 1
	v_add_u32_dpp v24, v24, v24 row_bcast:31 row_mask:0xc bank_mask:0xf
	s_and_saveexec_b64 s[50:51], s[82:83]
	ds_write_b32 v12, v24 offset:1280
	s_or_b64 exec, exec, s[50:51]
	v_mov_b32_e32 v25, 0
	v_mov_b32_e32 v26, 0
	s_waitcnt lgkmcnt(0)
	s_barrier
	s_and_saveexec_b64 s[50:51], s[84:85]
	ds_read_b32 v26, v195 offset:1280
	s_or_b64 exec, exec, s[50:51]
	s_and_saveexec_b64 s[50:51], s[86:87]
	ds_read_b32 v25, v195 offset:1284
	s_or_b64 exec, exec, s[50:51]
	v_mov_b32_e32 v27, 0
	v_mov_b32_e32 v28, 0
	s_and_saveexec_b64 s[50:51], s[88:89]
	ds_read_b32 v28, v195 offset:1288
	s_or_b64 exec, exec, s[50:51]
	s_and_saveexec_b64 s[50:51], s[90:91]
	ds_read_b32 v27, v195 offset:1292
	s_or_b64 exec, exec, s[50:51]
	v_mov_b32_e32 v29, 0
	v_mov_b32_e32 v30, 0
	s_and_saveexec_b64 s[50:51], s[92:93]
	ds_read_b32 v30, v195 offset:1296
	s_or_b64 exec, exec, s[50:51]
	s_and_saveexec_b64 s[50:51], s[94:95]
	ds_read_b32 v29, v195 offset:1300
	s_or_b64 exec, exec, s[50:51]
	v_mov_b32_e32 v31, 0
	v_mov_b32_e32 v32, 0
	s_and_saveexec_b64 s[50:51], s[96:97]
	ds_read_b32 v32, v195 offset:1304
	s_or_b64 exec, exec, s[50:51]
	s_and_saveexec_b64 s[50:51], s[38:39]
	ds_read_b32 v31, v195 offset:1308
	s_or_b64 exec, exec, s[50:51]
	v_sub_u32_e32 v23, v24, v23
	s_waitcnt lgkmcnt(0)
	v_add3_u32 v23, v23, v26, v25
	v_add3_u32 v23, v23, v28, v27
	v_add3_u32 v23, v23, v30, v29
	v_cndmask_b32_e64 v33, 0, 1, s[48:49]
	v_add3_u32 v23, v23, v32, v31
	v_cmp_lt_u32_e32 vcc, v23, v7
	v_add_u32_e32 v23, v23, v33
	v_cmp_gt_u32_e64 s[50:51], v14, v6
	s_and_b64 s[8:9], s[48:49], vcc
	v_cmp_lt_u32_e64 s[48:49], v23, v7
	v_add_u32_e32 v22, v23, v22
	s_or_b64 s[50:51], s[50:51], s[8:9]
	v_cmp_gt_u32_e32 vcc, v9, v6
	s_and_b64 s[8:9], s[44:45], s[48:49]
	v_cmp_lt_u32_e64 s[44:45], v22, v7
	v_add_u32_e32 v21, v22, v21
	s_or_b64 s[48:49], vcc, s[8:9]
	v_cmp_gt_u32_e32 vcc, v8, v6
	s_and_b64 s[8:9], s[42:43], s[44:45]
	v_cmp_lt_u32_e64 s[42:43], v21, v7
	s_or_b64 s[44:45], vcc, s[8:9]
	v_cmp_gt_u32_e32 vcc, v13, v6
	s_and_b64 s[8:9], s[40:41], s[42:43]
	v_cndmask_b32_e64 v24, 0, 1, s[50:51]
	v_cndmask_b32_e64 v25, 0, 1, s[48:49]
	s_or_b64 s[40:41], vcc, s[8:9]
	v_add_u32_e32 v23, v25, v24
	v_cndmask_b32_e64 v24, 0, 1, s[44:45]
	v_cndmask_b32_e64 v6, 0, 1, s[40:41]
	v_add3_u32 v21, v23, v24, v6
	s_waitcnt lgkmcnt(0)
	s_barrier
	v_mov_b32_e32 v15, v21
	s_nop 1
	v_add_u32_dpp v15, v15, v15 row_shr:1 row_mask:0xf bank_mask:0xf bound_ctrl:0
	s_nop 1
	v_add_u32_dpp v15, v15, v15 row_shr:2 row_mask:0xf bank_mask:0xf bound_ctrl:0
	s_nop 1
	v_add_u32_dpp v15, v15, v15 row_shr:4 row_mask:0xf bank_mask:0xf bound_ctrl:0
	s_nop 1
	v_add_u32_dpp v15, v15, v15 row_shr:8 row_mask:0xf bank_mask:0xf bound_ctrl:0
	s_nop 1
	v_add_u32_dpp v15, v15, v15 row_bcast:15 row_mask:0xa bank_mask:0xf
	s_nop 1
	v_add_u32_dpp v15, v15, v15 row_bcast:31 row_mask:0xc bank_mask:0xf
	s_and_saveexec_b64 s[42:43], s[82:83]
	ds_write_b32 v12, v15 offset:1280
	s_or_b64 exec, exec, s[42:43]
	v_mov_b32_e32 v16, 0
	v_mov_b32_e32 v17, 0
	s_waitcnt lgkmcnt(0)
	s_barrier
	s_and_saveexec_b64 s[42:43], s[84:85]
	ds_read_b32 v17, v195 offset:1280
	s_or_b64 exec, exec, s[42:43]
	s_and_saveexec_b64 s[42:43], s[86:87]
	ds_read_b32 v16, v195 offset:1284
	s_or_b64 exec, exec, s[42:43]
	v_mov_b32_e32 v18, 0
	v_mov_b32_e32 v19, 0
	s_and_saveexec_b64 s[42:43], s[88:89]
	ds_read_b32 v19, v195 offset:1288
	s_or_b64 exec, exec, s[42:43]
	s_and_saveexec_b64 s[42:43], s[90:91]
	ds_read_b32 v18, v195 offset:1292
	s_or_b64 exec, exec, s[42:43]
	v_mov_b32_e32 v20, 0
	v_mov_b32_e32 v22, 0
	s_and_saveexec_b64 s[42:43], s[92:93]
	ds_read_b32 v22, v195 offset:1296
	s_or_b64 exec, exec, s[42:43]
	s_and_saveexec_b64 s[42:43], s[94:95]
	ds_read_b32 v20, v195 offset:1300
	s_or_b64 exec, exec, s[42:43]
	v_mov_b32_e32 v23, 0
	v_mov_b32_e32 v24, 0
	s_and_saveexec_b64 s[42:43], s[96:97]
	ds_read_b32 v24, v195 offset:1304
	s_or_b64 exec, exec, s[42:43]
	s_and_saveexec_b64 s[42:43], s[38:39]
	ds_read_b32 v23, v195 offset:1308
	s_or_b64 exec, exec, s[42:43]
	s_and_b32 s8, s66, 15
	s_xor_b64 s[10:11], s[50:51], -1
	s_lshl_b32 s9, s8, 15
	v_lshl_add_u32 v6, s4, 11, v2
	s_add_u32 s42, s18, s9
	s_addc_u32 s43, s19, 0
	v_ashrrev_i32_e32 v7, 31, v6
	s_waitcnt lgkmcnt(0)
	s_barrier
	s_and_saveexec_b64 s[22:23], s[10:11]
	s_xor_b64 s[50:51], exec, s[22:23]
	s_cbranch_execz .LBB0_1589
	v_lshl_add_u64 v[26:27], v[6:7], 2, s[42:43]
	global_store_dword v[26:27], v248, off
